# p0 weight conversion in batches of four items (eight tile loads in flight, one barrier pair per batch)
# baseline (speedup 1.0000x reference)
.LBB0_20:
	s_or_b64 exec, exec, s[12:13]
	s_cmpk_gt_i32 s54, 0xfff
	s_cbranch_scc1 .LBB0_61
	s_add_u32 s3, s10, 0x517e0a00
	s_addc_u32 s9, s11, 0
	s_add_u32 s26, s10, 0x518e0a00
	s_addc_u32 s27, s11, 0
	s_add_u32 s28, s10, 0x4fee0a00
	s_addc_u32 s29, s11, 0
	s_add_u32 s30, s10, 0x4fce0a00
	s_addc_u32 s31, s11, 0
	s_add_u32 s33, s10, 0x4f8e0a00
	s_addc_u32 s34, s11, 0
	s_add_u32 s35, s10, 0x535e0a00
	s_addc_u32 s36, s11, 0
	s_add_u32 s37, s10, 0x4e6e0a00
	s_addc_u32 s38, s11, 0
	s_add_u32 s39, s10, 0x529e0a00
	s_addc_u32 s40, s11, 0
	v_lshlrev_b32_e32 v0, 2, v4
	s_add_u32 s41, s10, 0x4e0e0a00
	v_ashrrev_i32_e32 v13, 4, v4
	v_and_b32_e32 v0, 60, v0
	v_ashrrev_i32_e32 v6, 3, v4
	v_and_b32_e32 v2, 7, v4
	s_movk_i32 s10, 0x104
	v_lshl_add_u32 v1, v0, 2, 0
	v_lshlrev_b32_e32 v8, 3, v2
	v_lshl_add_u32 v3, v6, 2, 0
	v_bfe_u32 v24, v4, 1, 2
	v_lshlrev_b32_e32 v4, 5, v4
	v_and_b32_e32 v7, 31, v6
	v_mul_lo_u32 v16, v13, s10
	v_mul_u32_u24_e32 v2, 0x820, v2
	v_mov_b32_e32 v5, 0
	v_and_or_b32 v4, v4, 32, v7
	v_ashrrev_i32_e32 v7, 31, v6
	v_add_u32_e32 v25, v1, v16
	v_add_u32_e32 v28, v3, v2
	s_addc_u32 s42, s11, 0
	s_mov_b32 s11, 0
	v_lshlrev_b64 v[10:11], 10, v[6:7]
	v_mov_b32_e32 v9, v5
	v_lshlrev_b32_e32 v12, 3, v4
	s_add_i32 s43, 0, 0x27840
	s_add_i32 s44, 0, 0x27878
	s_add_i32 s45, 0, 0x27870
	s_add_i32 s46, 0, 0x27868
	s_add_i32 s47, 0, 0x27828
	s_add_i32 s48, 0, 0x27820
	s_add_i32 s49, 0, 0x27818
	v_lshlrev_b32_e32 v14, 2, v0
	v_mov_b32_e32 v15, v5
	v_add_u32_e32 v26, 0x2080, v25
	v_add_u32_e32 v27, 0x2088, v25
	v_add_u32_e32 v29, 0x400, v28
	s_mov_b32 s50, s54
	s_branch .Lw_batch
.LBB0_24:
	s_cmpk_gt_i32 s50, 0xeff
	s_mov_b64 s[12:13], -1
	s_cbranch_scc0 .LBB0_30
	s_cmpk_gt_u32 s50, 0xf7f
	s_cbranch_scc0 .LBB0_27
	s_add_i32 s10, s50, 0xfffff080
	s_lshr_b32 s10, s10, 4
	s_add_i32 s52, s10, 0x110
	s_mov_b64 s[12:13], 0

.LBB0_54:
	s_and_b32 s24, s51, s50
	s_lshl_b32 s10, s24, 6
	v_add_u32_e32 v4, s10, v13
	v_ashrrev_i32_e32 v0, 31, v4
	v_lshl_add_u64 v[16:17], s[18:19], 0, v[14:15]
	v_mul_lo_u32 v2, s22, v0
	v_mul_lo_u32 v3, s23, v4
	v_mad_u64_u32 v[0:1], s[18:19], s22, v4, 0
	v_add_u32_e32 v4, 32, v4
	v_add3_u32 v1, v1, v2, v3
	v_ashrrev_i32_e32 v18, 31, v4
	v_lshl_add_u64 v[0:1], v[0:1], 2, v[16:17]
	v_mul_lo_u32 v20, s22, v18
	v_mul_lo_u32 v21, s23, v4
	v_mad_u64_u32 v[18:19], s[18:19], s22, v4, 0
	v_add3_u32 v19, v19, v20, v21
	v_lshl_add_u64 v[16:17], v[18:19], 2, v[16:17]
	s_cmp_eq_u32 s77, 0
	s_cbranch_scc1 .Lw_ld0
	s_cmp_eq_u32 s77, 1
	s_cbranch_scc1 .Lw_ld1
	s_cmp_eq_u32 s77, 2
	s_cbranch_scc1 .Lw_ld2
.Lw_ld3:
	global_load_dwordx4 v[190:193], v[0:1], off
	global_load_dwordx4 v[194:197], v[16:17], off
	v_writelane_b32 v198, s12, 33
	v_writelane_b32 v198, s13, 34
	v_writelane_b32 v198, s16, 35
	v_writelane_b32 v198, s17, 36
	v_writelane_b32 v198, s20, 37
	v_writelane_b32 v198, s21, 38
	v_writelane_b32 v198, s14, 39
	v_writelane_b32 v198, s15, 40
	v_writelane_b32 v198, s53, 41
	v_writelane_b32 v198, s24, 42
	v_writelane_b32 v198, s10, 43
	s_branch .Lw_ldn
.Lw_ld0:
	global_load_dwordx4 v[40:43], v[0:1], off
	global_load_dwordx4 v[44:47], v[16:17], off
	v_writelane_b32 v198, s12, 0
	v_writelane_b32 v198, s13, 1
	v_writelane_b32 v198, s16, 2
	v_writelane_b32 v198, s17, 3
	v_writelane_b32 v198, s20, 4
	v_writelane_b32 v198, s21, 5
	v_writelane_b32 v198, s14, 6
	v_writelane_b32 v198, s15, 7
	v_writelane_b32 v198, s53, 8
	v_writelane_b32 v198, s24, 9
	v_writelane_b32 v198, s10, 10
	s_branch .Lw_ldn
.Lw_ld1:
	global_load_dwordx4 v[48:51], v[0:1], off
	global_load_dwordx4 v[52:55], v[16:17], off
	v_writelane_b32 v198, s12, 11
	v_writelane_b32 v198, s13, 12
	v_writelane_b32 v198, s16, 13
	v_writelane_b32 v198, s17, 14
	v_writelane_b32 v198, s20, 15
	v_writelane_b32 v198, s21, 16
	v_writelane_b32 v198, s14, 17
	v_writelane_b32 v198, s15, 18
	v_writelane_b32 v198, s53, 19
	v_writelane_b32 v198, s24, 20
	v_writelane_b32 v198, s10, 21
	s_branch .Lw_ldn
.Lw_ld2:
	global_load_dwordx4 v[56:59], v[0:1], off
	global_load_dwordx4 v[60:63], v[16:17], off
	v_writelane_b32 v198, s12, 22
	v_writelane_b32 v198, s13, 23
	v_writelane_b32 v198, s16, 24
	v_writelane_b32 v198, s17, 25
	v_writelane_b32 v198, s20, 26
	v_writelane_b32 v198, s21, 27
	v_writelane_b32 v198, s14, 28
	v_writelane_b32 v198, s15, 29
	v_writelane_b32 v198, s53, 30
	v_writelane_b32 v198, s24, 31
	v_writelane_b32 v198, s10, 32
.Lw_ldn:
	s_add_i32 s77, s77, 1
	s_add_i32 s50, s50, s8
	s_cmpk_gt_i32 s50, 0xfff
	s_cbranch_scc1 .Lw_pa
	s_cmp_lt_u32 s77, 4
	s_cbranch_scc1 .LBB0_24
.Lw_pa:
	s_cmp_eq_u32 s77, 4
	s_cbranch_scc1 .Lw_pa_full
	s_waitcnt vmcnt(0)
.Lw_pa_full:
	s_waitcnt vmcnt(6)
	ds_write2_b32 v25, v40, v41 offset1:1
	ds_write2_b32 v25, v42, v43 offset0:2 offset1:3
	ds_write2_b32 v26, v44, v45 offset1:1
	ds_write2_b32 v27, v46, v47 offset1:1
	s_cmp_lt_u32 s77, 2
	s_cbranch_scc1 .Lw_pa_done
	s_waitcnt vmcnt(4)
	v_add_u32_e32 v199, 0x4100, v25
	v_add_u32_e32 v200, 0x4100, v26
	v_add_u32_e32 v201, 0x4100, v27
	ds_write2_b32 v199, v48, v49 offset1:1
	ds_write2_b32 v199, v50, v51 offset0:2 offset1:3
	ds_write2_b32 v200, v52, v53 offset1:1
	ds_write2_b32 v201, v54, v55 offset1:1
	s_cmp_lt_u32 s77, 3
	s_cbranch_scc1 .Lw_pa_done
	s_waitcnt vmcnt(2)
	v_add_u32_e32 v199, 0x8200, v25
	v_add_u32_e32 v200, 0x8200, v26
	v_add_u32_e32 v201, 0x8200, v27
	ds_write2_b32 v199, v56, v57 offset1:1
	ds_write2_b32 v199, v58, v59 offset0:2 offset1:3
	ds_write2_b32 v200, v60, v61 offset1:1
	ds_write2_b32 v201, v62, v63 offset1:1
	s_cmp_lt_u32 s77, 4
	s_cbranch_scc1 .Lw_pa_done
	s_waitcnt vmcnt(0)
	v_add_u32_e32 v199, 0xc300, v25
	v_add_u32_e32 v200, 0xc300, v26
	v_add_u32_e32 v201, 0xc300, v27
	ds_write2_b32 v199, v190, v191 offset1:1
	ds_write2_b32 v199, v192, v193 offset0:2 offset1:3
	ds_write2_b32 v200, v194, v195 offset1:1
	ds_write2_b32 v201, v196, v197 offset1:1
.Lw_pa_done:
	s_waitcnt lgkmcnt(0)
	s_barrier
	s_mov_b32 s76, 0
.Lw_pb_loop:
	s_cmp_eq_u32 s76, 0
	s_cbranch_scc1 .Lw_rs0
	s_cmp_eq_u32 s76, 1
	s_cbranch_scc1 .Lw_rs1
	s_cmp_eq_u32 s76, 2
	s_cbranch_scc1 .Lw_rs2
.Lw_rs3:
	v_readlane_b32 s12, v198, 33
	v_readlane_b32 s13, v198, 34
	v_readlane_b32 s16, v198, 35
	v_readlane_b32 s17, v198, 36
	v_readlane_b32 s20, v198, 37
	v_readlane_b32 s21, v198, 38
	v_readlane_b32 s14, v198, 39
	v_readlane_b32 s15, v198, 40
	v_readlane_b32 s53, v198, 41
	v_readlane_b32 s24, v198, 42
	v_readlane_b32 s10, v198, 43
	s_branch .Lw_rsn
.Lw_rs0:
	v_readlane_b32 s12, v198, 0
	v_readlane_b32 s13, v198, 1
	v_readlane_b32 s16, v198, 2
	v_readlane_b32 s17, v198, 3
	v_readlane_b32 s20, v198, 4
	v_readlane_b32 s21, v198, 5
	v_readlane_b32 s14, v198, 6
	v_readlane_b32 s15, v198, 7
	v_readlane_b32 s53, v198, 8
	v_readlane_b32 s24, v198, 9
	v_readlane_b32 s10, v198, 10
	s_branch .Lw_rsn
.Lw_rs1:
	v_readlane_b32 s12, v198, 11
	v_readlane_b32 s13, v198, 12
	v_readlane_b32 s16, v198, 13
	v_readlane_b32 s17, v198, 14
	v_readlane_b32 s20, v198, 15
	v_readlane_b32 s21, v198, 16
	v_readlane_b32 s14, v198, 17
	v_readlane_b32 s15, v198, 18
	v_readlane_b32 s53, v198, 19
	v_readlane_b32 s24, v198, 20
	v_readlane_b32 s10, v198, 21
	s_branch .Lw_rsn
.Lw_rs2:
	v_readlane_b32 s12, v198, 22
	v_readlane_b32 s13, v198, 23
	v_readlane_b32 s16, v198, 24
	v_readlane_b32 s17, v198, 25
	v_readlane_b32 s20, v198, 26
	v_readlane_b32 s21, v198, 27
	v_readlane_b32 s14, v198, 28
	v_readlane_b32 s15, v198, 29
	v_readlane_b32 s53, v198, 30
	v_readlane_b32 s24, v198, 31
	v_readlane_b32 s10, v198, 32
.Lw_rsn:
	s_mul_i32 s78, s76, 0x4100
	s_nop 1
	v_add_u32_e32 v202, s78, v28
	v_add_u32_e32 v203, 0x400, v202
	ds_read2_b32 v[18:19], v202 offset1:65
	ds_read2_b32 v[22:23], v202 offset0:130 offset1:195
	ds_read2_b32 v[20:21], v203 offset0:4 offset1:69
	ds_read2_b32 v[16:17], v203 offset0:134 offset1:199
	s_waitcnt lgkmcnt(3)
	v_cvt_pk_bf16_f32 v0, v18, v19
	s_waitcnt lgkmcnt(2)
	v_cvt_pk_bf16_f32 v1, v22, v23
	s_waitcnt lgkmcnt(1)
	v_cvt_pk_bf16_f32 v2, v20, v21
	s_waitcnt lgkmcnt(0)
	v_cvt_pk_bf16_f32 v3, v16, v17
	s_cmp_eq_u64 s[16:17], 0
	s_cbranch_scc1 .Lw_v57
	v_lshlrev_b32_e32 v30, 16, v0
	v_and_b32_e32 v31, 0xffff0000, v0
	v_lshlrev_b32_e32 v32, 16, v1
	v_and_b32_e32 v33, 0xffff0000, v1
	v_add_u32_e32 v4, s53, v6
	v_pk_add_f32 v[30:31], v[18:19], v[30:31] neg_lo:[0,1] neg_hi:[0,1]
	v_pk_add_f32 v[32:33], v[22:23], v[32:33] neg_lo:[0,1] neg_hi:[0,1]
	v_lshrrev_b32_e32 v4, 1, v4
	v_cvt_pk_bf16_f32 v30, v30, v31
	v_cvt_pk_bf16_f32 v31, v32, v33
	v_lshlrev_b32_e32 v32, 16, v2
	v_and_b32_e32 v33, 0xffff0000, v2
	v_lshlrev_b32_e32 v34, 16, v3
	v_and_b32_e32 v35, 0xffff0000, v3
	v_and_b32_e32 v4, 0x3ffffff0, v4
	v_pk_add_f32 v[32:33], v[20:21], v[32:33] neg_lo:[0,1] neg_hi:[0,1]
	v_pk_add_f32 v[34:35], v[16:17], v[34:35] neg_lo:[0,1] neg_hi:[0,1]
	v_or_b32_e32 v4, s24, v4
	v_cvt_pk_bf16_f32 v32, v32, v33
	v_cvt_pk_bf16_f32 v33, v34, v35
	v_lshl_or_b32 v34, v4, 2, v24
	v_ashrrev_i32_e32 v35, 31, v34
	v_lshlrev_b64 v[34:35], 10, v[34:35]
	v_lshl_or_b32 v34, v12, 1, v34
	v_lshl_add_u64 v[36:37], s[12:13], 0, v[34:35]
	v_lshl_add_u64 v[34:35], s[16:17], 0, v[34:35]
	global_store_dwordx4 v[36:37], v[0:3], off
	global_store_dwordx4 v[34:35], v[30:33], off
	s_branch .Lw_pb_ret
.Lw_v57:
	s_cmp_eq_u64 s[20:21], 0
	s_cbranch_scc1 .Lw_v22
	v_mul_f32_e32 v4, 0x42800000, v18
	v_mul_f32_e32 v19, 0x42800000, v19
	v_mov_b32_e32 v18, 0
	v_cvt_pk_fp8_f32 v18, v4, v19
	v_mul_f32_e32 v4, 0x42800000, v20
	v_mul_f32_e32 v20, 0x42800000, v21
	v_mov_b32_e32 v19, 0
	v_cvt_pk_fp8_f32 v19, v4, v20
	v_mul_f32_e32 v22, 0x42800000, v22
	v_mul_f32_e32 v23, 0x42800000, v23
	v_mul_f32_e32 v4, 0x42800000, v16
	v_mul_f32_e32 v16, 0x42800000, v17
	v_cvt_pk_fp8_f32 v18, v22, v23 op_sel:[0,0,1]
	v_cvt_pk_fp8_f32 v19, v4, v16 op_sel:[0,0,1]
	v_lshl_add_u64 v[16:17], s[20:21], 0, v[10:11]
	v_lshl_add_u64 v[16:17], v[16:17], 0, s[10:11]
	v_lshl_add_u64 v[16:17], v[16:17], 0, v[8:9]
	global_store_dwordx2 v[16:17], v[18:19], off
	s_branch .Lw_pb_ret

.Lw_pb_ret:
	s_add_i32 s76, s76, 1
	s_cmp_lt_u32 s76, s77
	s_cbranch_scc1 .Lw_pb_loop
	s_barrier
	s_cmpk_gt_i32 s50, 0xfff
	s_cbranch_scc1 .LBB0_61
.Lw_batch:
	s_mov_b32 s77, 0
	s_branch .LBB0_24
